# P2 token loop: next token's latent row + position prefetched one trip ahead, rope-key gains loaded once before the loop, counted vmcnt(6) instead of vmcnt(0)
# speedup vs baseline: 1.0005x; 1.0005x over previous
; __global__ void __launch_bounds__(512, 2) fwd_kernel(Params p) {
;     ...
;         for (int blk = vcu; blk < T / 64; blk += G) {
;             {
;                 const int tt = wave & 1, kq = wave >> 1, j = lane & 31, hh = lane >> 5;
;                 const bf16_t* hr = Hb + (size_t)(blk * 64 + tt * 32 + j) * DM + kq * 512 + hh * 8;
;                 const bf16_t* w0 = WkrT + (size_t)j * DM + kq * 512 + hh * 8; const bf16_t* w1 = w0 + (size_t)32 * DM;
;                 f32x16 a0 = {}, a1 = {};
;                 bf16x8 hb[32], b0[2][4], b1[2][4];
; #pragma unroll
;                 for (int i = 0; i < 32; ++i) hb[i] = *(const bf16x8*)(hr + i * 16);
; #pragma unroll
;                 for (int i = 0; i < 4; ++i) { b0[0][i] = *(const bf16x8*)(w0 + i * 16); b1[0][i] = *(const bf16x8*)(w1 + i * 16); }
; #pragma unroll
;                 for (int ch = 0; ch < 8; ++ch) {
;                     if (ch + 1 < 8) {
; #pragma unroll
;                         for (int i = 0; i < 4; ++i) { b0[(ch + 1) & 1][i] = *(const bf16x8*)(w0 + (ch + 1) * 64 + i * 16); b1[(ch + 1) & 1][i] = *(const bf16x8*)(w1 + (ch + 1) * 64 + i * 16); } }
; #pragma unroll
;                     for (int i = 0; i < 4; ++i) { a0 = __builtin_amdgcn_mfma_f32_32x32x16_bf16(b0[ch & 1][i], hb[ch * 4 + i], a0, 0, 0, 0); a1 = __builtin_amdgcn_mfma_f32_32x32x16_bf16(b1[ch & 1][i], hb[ch * 4 + i], a1, 0, 0, 0); }
;                 }
.LBB0_230:
	global_load_dwordx4 v[0:3], v[38:39], off
	v_lshl_or_b32 v4, s45, 6, v109
	v_ashrrev_i32_e32 v5, 31, v4
	v_lshlrev_b64 v[4:5], 12, v[4:5]
	v_lshl_add_u64 v[112:113], v[34:35], 0, v[4:5]
	global_load_dwordx4 v[16:19], v[112:113], off
	global_load_dwordx4 v[20:23], v[40:41], off
	global_load_dwordx4 v[114:117], v[38:39], off offset:32
	global_load_dwordx4 v[140:143], v[112:113], off offset:32
	global_load_dwordx4 v[144:147], v[46:47], off
	global_load_dwordx4 v[148:151], v[38:39], off offset:64
	global_load_dwordx4 v[152:155], v[112:113], off offset:64
	s_ashr_i32 s27, s26, 31
	s_lshl_b64 s[10:11], s[26:27], 8
	s_lshl_b64 s[52:53], s[26:27], 2
	s_waitcnt vmcnt(6)
	v_mfma_f32_32x32x16_bf16 v[0:15], v[0:3], v[16:19], 0
	s_waitcnt vmcnt(3)
	v_mfma_f32_32x32x16_bf16 v[0:15], v[114:117], v[140:143], v[0:15]
	global_load_dwordx4 v[114:117], v[48:49], off
	global_load_dwordx4 v[156:159], v[38:39], off offset:96
	v_mfma_f32_32x32x16_bf16 v[16:31], v[20:23], v[16:19], 0
	s_waitcnt vmcnt(4)
	v_mfma_f32_32x32x16_bf16 v[16:31], v[144:147], v[140:143], v[16:31]
	global_load_dwordx4 v[140:143], v[112:113], off offset:96
	s_waitcnt vmcnt(3)
	v_mfma_f32_32x32x16_bf16 v[0:15], v[148:151], v[152:155], v[0:15]
	global_load_dwordx4 v[144:147], v[50:51], off
	global_load_dwordx4 v[148:151], v[38:39], off offset:128
	s_waitcnt vmcnt(4)
	v_mfma_f32_32x32x16_bf16 v[16:31], v[114:117], v[152:155], v[16:31]
	global_load_dwordx4 v[114:117], v[112:113], off offset:128
	s_waitcnt vmcnt(3)
	v_mfma_f32_32x32x16_bf16 v[0:15], v[156:159], v[140:143], v[0:15]
	global_load_dwordx4 v[152:155], v[52:53], off
	global_load_dwordx4 v[156:159], v[38:39], off offset:160
	s_waitcnt vmcnt(4)
	v_mfma_f32_32x32x16_bf16 v[16:31], v[144:147], v[140:143], v[16:31]
	global_load_dwordx4 v[140:143], v[112:113], off offset:160
	s_waitcnt vmcnt(3)
	v_mfma_f32_32x32x16_bf16 v[0:15], v[148:151], v[114:117], v[0:15]
	global_load_dwordx4 v[144:147], v[54:55], off
	global_load_dwordx4 v[148:151], v[38:39], off offset:192
	s_waitcnt vmcnt(4)
	v_mfma_f32_32x32x16_bf16 v[16:31], v[152:155], v[114:117], v[16:31]
	global_load_dwordx4 v[114:117], v[112:113], off offset:192
	s_waitcnt vmcnt(3)
	v_mfma_f32_32x32x16_bf16 v[0:15], v[156:159], v[140:143], v[0:15]
	global_load_dwordx4 v[152:155], v[56:57], off
	global_load_dwordx4 v[156:159], v[38:39], off offset:224
	s_waitcnt vmcnt(4)
	v_mfma_f32_32x32x16_bf16 v[16:31], v[144:147], v[140:143], v[16:31]
	global_load_dwordx4 v[140:143], v[112:113], off offset:224
	s_waitcnt vmcnt(3)
	v_mfma_f32_32x32x16_bf16 v[0:15], v[148:151], v[114:117], v[0:15]
	global_load_dwordx4 v[144:147], v[58:59], off
	global_load_dwordx4 v[148:151], v[38:39], off offset:256
	s_waitcnt vmcnt(4)
	v_mfma_f32_32x32x16_bf16 v[16:31], v[152:155], v[114:117], v[16:31]
	global_load_dwordx4 v[114:117], v[112:113], off offset:256
	s_waitcnt vmcnt(3)
	v_mfma_f32_32x32x16_bf16 v[0:15], v[156:159], v[140:143], v[0:15]
	global_load_dwordx4 v[152:155], v[60:61], off
	global_load_dwordx4 v[156:159], v[38:39], off offset:288
	s_waitcnt vmcnt(4)
	v_mfma_f32_32x32x16_bf16 v[16:31], v[144:147], v[140:143], v[16:31]
	global_load_dwordx4 v[140:143], v[112:113], off offset:288
	s_waitcnt vmcnt(3)
	v_mfma_f32_32x32x16_bf16 v[0:15], v[148:151], v[114:117], v[0:15]
	global_load_dwordx4 v[144:147], v[62:63], off
	global_load_dwordx4 v[148:151], v[38:39], off offset:320
	s_waitcnt vmcnt(4)
	v_mfma_f32_32x32x16_bf16 v[16:31], v[152:155], v[114:117], v[16:31]
	global_load_dwordx4 v[114:117], v[112:113], off offset:320
	s_waitcnt vmcnt(3)
	v_mfma_f32_32x32x16_bf16 v[0:15], v[156:159], v[140:143], v[0:15]
	global_load_dwordx4 v[152:155], v[64:65], off
	global_load_dwordx4 v[156:159], v[38:39], off offset:352
	s_waitcnt vmcnt(4)
	v_mfma_f32_32x32x16_bf16 v[16:31], v[144:147], v[140:143], v[16:31]
	global_load_dwordx4 v[140:143], v[112:113], off offset:352
	s_waitcnt vmcnt(3)
	v_mfma_f32_32x32x16_bf16 v[0:15], v[148:151], v[114:117], v[0:15]
	global_load_dwordx4 v[144:147], v[66:67], off
	global_load_dwordx4 v[148:151], v[38:39], off offset:384
	s_waitcnt vmcnt(4)
	v_mfma_f32_32x32x16_bf16 v[16:31], v[152:155], v[114:117], v[16:31]
	global_load_dwordx4 v[114:117], v[112:113], off offset:384
	s_waitcnt vmcnt(3)
	v_mfma_f32_32x32x16_bf16 v[0:15], v[156:159], v[140:143], v[0:15]
	global_load_dwordx4 v[152:155], v[68:69], off
	global_load_dwordx4 v[156:159], v[38:39], off offset:416
	s_waitcnt vmcnt(4)
	v_mfma_f32_32x32x16_bf16 v[16:31], v[144:147], v[140:143], v[16:31]
	global_load_dwordx4 v[140:143], v[112:113], off offset:416
	s_waitcnt vmcnt(3)
	v_mfma_f32_32x32x16_bf16 v[0:15], v[148:151], v[114:117], v[0:15]
	global_load_dwordx4 v[144:147], v[70:71], off
	global_load_dwordx4 v[148:151], v[38:39], off offset:448
	s_waitcnt vmcnt(4)
	v_mfma_f32_32x32x16_bf16 v[16:31], v[152:155], v[114:117], v[16:31]
	global_load_dwordx4 v[114:117], v[112:113], off offset:448
	s_waitcnt vmcnt(3)
	v_mfma_f32_32x32x16_bf16 v[0:15], v[156:159], v[140:143], v[0:15]
	global_load_dwordx4 v[152:155], v[72:73], off
	global_load_dwordx4 v[156:159], v[38:39], off offset:480
	s_waitcnt vmcnt(4)
	v_mfma_f32_32x32x16_bf16 v[16:31], v[144:147], v[140:143], v[16:31]
	global_load_dwordx4 v[140:143], v[112:113], off offset:480
	s_waitcnt vmcnt(3)
	v_mfma_f32_32x32x16_bf16 v[0:15], v[148:151], v[114:117], v[0:15]
	global_load_dwordx4 v[144:147], v[74:75], off
	global_load_dwordx4 v[148:151], v[38:39], off offset:512
	s_waitcnt vmcnt(4)
	v_mfma_f32_32x32x16_bf16 v[16:31], v[152:155], v[114:117], v[16:31]
	global_load_dwordx4 v[114:117], v[112:113], off offset:512
	s_waitcnt vmcnt(3)
; __global__ void __launch_bounds__(512, 2) fwd_kernel(Params p) {
;     ...
;                 for (int ch = 0; ch < 8; ++ch) {
;                     if (ch + 1 < 8) {
; #pragma unroll
;                         for (int i = 0; i < 4; ++i) { b0[(ch + 1) & 1][i] = *(const bf16x8*)(w0 + (ch + 1) * 64 + i * 16); b1[(ch + 1) & 1][i] = *(const bf16x8*)(w1 + (ch + 1) * 64 + i * 16); } }
; #pragma unroll
;                     for (int i = 0; i < 4; ++i) { a0 = __builtin_amdgcn_mfma_f32_32x32x16_bf16(b0[ch & 1][i], hb[ch * 4 + i], a0, 0, 0, 0); a1 = __builtin_amdgcn_mfma_f32_32x32x16_bf16(b1[ch & 1][i], hb[ch * 4 + i], a1, 0, 0, 0); }
;                 }
;                 LAS float* pp = zk + (kq * 64 + tt * 32 + j) * 65;
; #pragma unroll
;                 for (int r = 0; r < 16; ++r) { const int c = (r & 3) + 8 * (r >> 2) + 4 * hh; pp[c] = a0[r]; pp[32 + c] = a1[r]; }
;             }
;             __syncthreads();
;     ...
;                 const bf16_t* zr = Zb + (size_t)m * ZLD;
;                 {
;                     const u32x2 zq = *(const u32x2*)(Z8 + (size_t)m * 1024 + lane * 8), zkv = *(const u32x2*)(Z8 + (size_t)m * 1024 + 512 + lane * 8);
;                     const f32x2 q0 = __builtin_amdgcn_cvt_pk_f32_fp8((int)zq.x, false), q1 = __builtin_amdgcn_cvt_pk_f32_fp8((int)zq.x, true), q2 = __builtin_amdgcn_cvt_pk_f32_fp8((int)zq.y, false), q3 = __builtin_amdgcn_cvt_pk_f32_fp8((int)zq.y, true);
;                     const f32x2 k0 = __builtin_amdgcn_cvt_pk_f32_fp8((int)zkv.x, false), k1 = __builtin_amdgcn_cvt_pk_f32_fp8((int)zkv.x, true), k2 = __builtin_amdgcn_cvt_pk_f32_fp8((int)zkv.y, false), k3 = __builtin_amdgcn_cvt_pk_f32_fp8((int)zkv.y, true);
;                     const float vq[8] = {q0.x, q0.y, q1.x, q1.y, q2.x, q2.y, q3.x, q3.y};
;                     const float vk[8] = {k0.x, k0.y, k1.x, k1.y, k2.x, k2.y, k3.x, k3.y};
;                     float sq = 0.f, sk = 0.f;
; #pragma unroll
;                     for (int q = 0; q < 8; ++q) { sq += vq[q] * vq[q]; sk += vk[q] * vk[q]; }
;                     sq = wave_sum(sq); sk = wave_sum(sk);
;                     if (lane == 0) { RSQ[m] = rsqrtf(sq * (1.f / 512.f) + RMS_EPS); RSKV[m] = rsqrtf(sk * (1.f / 512.f) + RMS_EPS); }
;                 }
;                 {
;                     const float pos = (float)((const int*)p.in[I_POS])[m];
;                     const int i = lane & 31;
	v_mfma_f32_32x32x16_bf16 v[0:15], v[156:159], v[140:143], v[0:15]
	global_load_dwordx4 v[152:155], v[76:77], off
	global_load_dwordx4 v[156:159], v[38:39], off offset:544
	s_waitcnt vmcnt(4)
	v_mfma_f32_32x32x16_bf16 v[16:31], v[144:147], v[140:143], v[16:31]
	global_load_dwordx4 v[140:143], v[112:113], off offset:544
	s_waitcnt vmcnt(3)
	v_mfma_f32_32x32x16_bf16 v[0:15], v[148:151], v[114:117], v[0:15]
	global_load_dwordx4 v[144:147], v[78:79], off
	global_load_dwordx4 v[148:151], v[38:39], off offset:576
	s_waitcnt vmcnt(4)
	v_mfma_f32_32x32x16_bf16 v[16:31], v[152:155], v[114:117], v[16:31]
	global_load_dwordx4 v[114:117], v[112:113], off offset:576
	s_waitcnt vmcnt(3)
	v_mfma_f32_32x32x16_bf16 v[0:15], v[156:159], v[140:143], v[0:15]
	global_load_dwordx4 v[152:155], v[80:81], off
	global_load_dwordx4 v[156:159], v[38:39], off offset:608
	s_waitcnt vmcnt(4)
	v_mfma_f32_32x32x16_bf16 v[16:31], v[144:147], v[140:143], v[16:31]
	global_load_dwordx4 v[140:143], v[112:113], off offset:608
	s_waitcnt vmcnt(3)
	v_mfma_f32_32x32x16_bf16 v[0:15], v[148:151], v[114:117], v[0:15]
	global_load_dwordx4 v[144:147], v[82:83], off
	global_load_dwordx4 v[148:151], v[38:39], off offset:640
	s_waitcnt vmcnt(4)
	v_mfma_f32_32x32x16_bf16 v[16:31], v[152:155], v[114:117], v[16:31]
	global_load_dwordx4 v[114:117], v[112:113], off offset:640
	s_waitcnt vmcnt(3)
	v_mfma_f32_32x32x16_bf16 v[0:15], v[156:159], v[140:143], v[0:15]
	global_load_dwordx4 v[152:155], v[84:85], off
	global_load_dwordx4 v[156:159], v[38:39], off offset:672
	s_waitcnt vmcnt(4)
	v_mfma_f32_32x32x16_bf16 v[16:31], v[144:147], v[140:143], v[16:31]
	global_load_dwordx4 v[140:143], v[112:113], off offset:672
	s_waitcnt vmcnt(3)
	v_mfma_f32_32x32x16_bf16 v[0:15], v[148:151], v[114:117], v[0:15]
	global_load_dwordx4 v[144:147], v[86:87], off
	global_load_dwordx4 v[148:151], v[38:39], off offset:704
	s_waitcnt vmcnt(4)
	v_mfma_f32_32x32x16_bf16 v[16:31], v[152:155], v[114:117], v[16:31]
	global_load_dwordx4 v[114:117], v[112:113], off offset:704
	s_waitcnt vmcnt(3)
	v_mfma_f32_32x32x16_bf16 v[0:15], v[156:159], v[140:143], v[0:15]
	global_load_dwordx4 v[152:155], v[88:89], off
	global_load_dwordx4 v[156:159], v[38:39], off offset:736
	s_waitcnt vmcnt(4)
	v_mfma_f32_32x32x16_bf16 v[16:31], v[144:147], v[140:143], v[16:31]
	global_load_dwordx4 v[140:143], v[112:113], off offset:736
	s_waitcnt vmcnt(3)
	v_mfma_f32_32x32x16_bf16 v[0:15], v[148:151], v[114:117], v[0:15]
	global_load_dwordx4 v[144:147], v[90:91], off
	global_load_dwordx4 v[148:151], v[38:39], off offset:768
	s_waitcnt vmcnt(4)
	v_mfma_f32_32x32x16_bf16 v[16:31], v[152:155], v[114:117], v[16:31]
	global_load_dwordx4 v[114:117], v[112:113], off offset:768
	s_waitcnt vmcnt(3)
	v_mfma_f32_32x32x16_bf16 v[0:15], v[156:159], v[140:143], v[0:15]
	global_load_dwordx4 v[152:155], v[92:93], off
	global_load_dwordx4 v[156:159], v[38:39], off offset:800
	s_waitcnt vmcnt(4)
	v_mfma_f32_32x32x16_bf16 v[16:31], v[144:147], v[140:143], v[16:31]
	global_load_dwordx4 v[140:143], v[112:113], off offset:800
	s_waitcnt vmcnt(3)
	v_mfma_f32_32x32x16_bf16 v[0:15], v[148:151], v[114:117], v[0:15]
	global_load_dwordx4 v[144:147], v[94:95], off
	global_load_dwordx4 v[148:151], v[38:39], off offset:832
	s_waitcnt vmcnt(4)
	v_mfma_f32_32x32x16_bf16 v[16:31], v[152:155], v[114:117], v[16:31]
	global_load_dwordx4 v[114:117], v[112:113], off offset:832
	s_waitcnt vmcnt(3)
	v_mfma_f32_32x32x16_bf16 v[0:15], v[156:159], v[140:143], v[0:15]
	global_load_dwordx4 v[152:155], v[96:97], off
	global_load_dwordx4 v[156:159], v[38:39], off offset:864
	s_waitcnt vmcnt(4)
	v_mfma_f32_32x32x16_bf16 v[16:31], v[144:147], v[140:143], v[16:31]
	global_load_dwordx4 v[140:143], v[112:113], off offset:864
	s_waitcnt vmcnt(3)
	v_mfma_f32_32x32x16_bf16 v[0:15], v[148:151], v[114:117], v[0:15]
	global_load_dwordx4 v[144:147], v[98:99], off
	global_load_dwordx4 v[148:151], v[38:39], off offset:896
	s_waitcnt vmcnt(4)
	v_mfma_f32_32x32x16_bf16 v[16:31], v[152:155], v[114:117], v[16:31]
	global_load_dwordx4 v[114:117], v[112:113], off offset:896
	global_load_dwordx4 v[152:155], v[100:101], off
	s_waitcnt vmcnt(4)
	v_mfma_f32_32x32x16_bf16 v[0:15], v[156:159], v[140:143], v[0:15]
	s_waitcnt vmcnt(3)
	v_mfma_f32_32x32x16_bf16 v[16:31], v[144:147], v[140:143], v[16:31]
	global_load_dwordx4 v[140:143], v[38:39], off offset:928
	global_load_dwordx4 v[144:147], v[112:113], off offset:928
	s_waitcnt vmcnt(3)
	v_mfma_f32_32x32x16_bf16 v[0:15], v[148:151], v[114:117], v[0:15]
	global_load_dwordx4 v[148:151], v[102:103], off
	global_load_dwordx4 v[156:159], v[38:39], off offset:960
	s_waitcnt vmcnt(4)
	v_mfma_f32_32x32x16_bf16 v[16:31], v[152:155], v[114:117], v[16:31]
	global_load_dwordx4 v[114:117], v[112:113], off offset:960
	s_waitcnt vmcnt(3)
	v_mfma_f32_32x32x16_bf16 v[0:15], v[140:143], v[144:147], v[0:15]
	global_load_dwordx4 v[140:143], v[104:105], off
	s_waitcnt vmcnt(3)
	v_mfma_f32_32x32x16_bf16 v[16:31], v[148:151], v[144:147], v[16:31]
	global_load_dwordx4 v[144:147], v[38:39], off offset:992
	global_load_dwordx4 v[148:151], v[112:113], off offset:992
	global_load_dwordx4 v[152:155], v[106:107], off
	v_mov_b32_e32 v113, s11
	v_or_b32_e32 v112, s10, v42
	s_lshl_b64 s[10:11], s[26:27], 6
	s_waitcnt vmcnt(4)
	v_mfma_f32_32x32x16_bf16 v[0:15], v[156:159], v[114:117], v[0:15]
	s_waitcnt vmcnt(3)
	v_mfma_f32_32x32x16_bf16 v[16:31], v[140:143], v[114:117], v[16:31]
	v_mov_b32_e32 v115, s11
	v_or_b32_e32 v114, s10, v108
	s_lshl_b64 s[10:11], s[26:27], 10
	v_lshl_add_u64 v[116:117], v[32:33], 0, s[10:11]
	s_mov_b32 s27, 0
	s_waitcnt vmcnt(1)
	v_mfma_f32_32x32x16_bf16 v[0:15], v[144:147], v[148:151], v[0:15]
	s_nop 11
	ds_write2_b32 v124, v0, v1 offset1:1
	s_waitcnt vmcnt(0)
	v_mfma_f32_32x32x16_bf16 v[16:31], v[152:155], v[148:151], v[16:31]
	s_nop 11
	ds_write2_b32 v124, v16, v17 offset0:32 offset1:33
	ds_write2_b32 v124, v2, v3 offset0:2 offset1:3
	ds_write2_b32 v124, v18, v19 offset0:34 offset1:35
	ds_write2_b32 v124, v4, v5 offset0:8 offset1:9
	ds_write2_b32 v124, v20, v21 offset0:40 offset1:41
	ds_write2_b32 v124, v6, v7 offset0:10 offset1:11
	ds_write2_b32 v124, v22, v23 offset0:42 offset1:43
	ds_write2_b32 v124, v8, v9 offset0:16 offset1:17
	ds_write2_b32 v124, v24, v25 offset0:48 offset1:49
	ds_write2_b32 v124, v10, v11 offset0:18 offset1:19
	ds_write2_b32 v124, v26, v27 offset0:50 offset1:51
	ds_write2_b32 v124, v12, v13 offset0:24 offset1:25
	ds_write2_b32 v124, v28, v29 offset0:56 offset1:57
	ds_write2_b32 v124, v14, v15 offset0:26 offset1:27
	ds_write2_b32 v124, v30, v31 offset0:58 offset1:59
	s_waitcnt lgkmcnt(0)
	v_lshl_add_u64 v[226:227], s[28:29], 0, v[116:117]
	v_add_co_u32_e32 v226, vcc, 0x25800000, v226
	s_add_u32 s10, s24, s52
	s_addc_u32 s11, s25, s53
	v_addc_co_u32_e32 v227, vcc, 0, v227, vcc
	global_load_dwordx2 v[220:221], v[226:227], off
	global_load_dwordx2 v[222:223], v[226:227], off offset:512
	global_load_dword v224, v37, s[10:11]
	global_load_dword v228, v[44:45], off
	global_load_dword v229, v[44:45], off offset:128
	s_barrier
; __global__ void __launch_bounds__(512, 2) fwd_kernel(Params p) {
;     ...
;             __syncthreads();
;             const float inv_freq = powf(10000.0f, -(float)(2 * (lane & 31)) / 64.0f);
; #pragma unroll 1
;             for (int tl = wave * 8; tl < wave * 8 + 8; ++tl) {
	s_waitcnt vmcnt(0)
	s_branch .LBB0_232

; __global__ void __launch_bounds__(512, 2) fwd_kernel(Params p) {
;     ...
;             for (int tl = wave * 8; tl < wave * 8 + 8; ++tl) {
;                 const int m = blk * 64 + tl;
;                 const bf16_t* zr = Zb + (size_t)m * ZLD;
;                 {
;                     const u32x2 zq = *(const u32x2*)(Z8 + (size_t)m * 1024 + lane * 8), zkv = *(const u32x2*)(Z8 + (size_t)m * 1024 + 512 + lane * 8);
;                     const f32x2 q0 = __builtin_amdgcn_cvt_pk_f32_fp8((int)zq.x, false), q1 = __builtin_amdgcn_cvt_pk_f32_fp8((int)zq.x, true), q2 = __builtin_amdgcn_cvt_pk_f32_fp8((int)zq.y, false), q3 = __builtin_amdgcn_cvt_pk_f32_fp8((int)zq.y, true);
;                     const f32x2 k0 = __builtin_amdgcn_cvt_pk_f32_fp8((int)zkv.x, false), k1 = __builtin_amdgcn_cvt_pk_f32_fp8((int)zkv.x, true), k2 = __builtin_amdgcn_cvt_pk_f32_fp8((int)zkv.y, false), k3 = __builtin_amdgcn_cvt_pk_f32_fp8((int)zkv.y, true);
;                     const float vq[8] = {q0.x, q0.y, q1.x, q1.y, q2.x, q2.y, q3.x, q3.y};
;                     const float vk[8] = {k0.x, k0.y, k1.x, k1.y, k2.x, k2.y, k3.x, k3.y};
;                     float sq = 0.f, sk = 0.f;
; #pragma unroll
;                     for (int q = 0; q < 8; ++q) { sq += vq[q] * vq[q]; sk += vk[q] * vk[q]; }
;                     sq = wave_sum(sq); sk = wave_sum(sk);
;                     if (lane == 0) { RSQ[m] = rsqrtf(sq * (1.f / 512.f) + RMS_EPS); RSKV[m] = rsqrtf(sk * (1.f / 512.f) + RMS_EPS); }
;                 }
;                 {
;                     const float pos = (float)((const int*)p.in[I_POS])[m];
;                     const int i = lane & 31;
;                     const float ang = pos * inv_freq; float sn, cs; sincosf(ang, &sn, &cs);
.LBB0_232:
	s_waitcnt vmcnt(6)
	v_mov_b32_e32 v2, v220
	v_mov_b32_e32 v3, v221
	v_mov_b32_e32 v0, v222
	v_mov_b32_e32 v1, v223
	v_mov_b32_e32 v225, v224
	s_cmpk_eq_i32 s27, 0x71c
	s_cbranch_scc1 .Lp2_tok_nopf
	v_lshl_add_u64 v[226:227], v[116:117], 0, s[50:51]
	s_add_u32 s10, s24, s52
	s_addc_u32 s11, s25, s53
	v_lshl_add_u64 v[226:227], s[28:29], 0, v[226:227]
	v_add_co_u32_e32 v226, vcc, 0x25800000, v226
	s_nop 1
	v_addc_co_u32_e32 v227, vcc, 0, v227, vcc
	global_load_dwordx2 v[220:221], v[226:227], off
	global_load_dwordx2 v[222:223], v[226:227], off offset:512
	global_load_dword v224, v37, s[10:11] offset:4
.Lp2_tok_nopf:
	v_cvt_pk_f32_fp8_e32 v[4:5], v2
	v_cvt_pk_f32_fp8_e32 v[10:11], v0
	s_waitcnt lgkmcnt(0)
	v_cvt_pk_f32_fp8_sdwa v[6:7], v2 src0_sel:WORD_1
	v_cvt_pk_f32_fp8_e32 v[8:9], v3
	v_cvt_pk_f32_fp8_sdwa v[2:3], v3 src0_sel:WORD_1
	v_cvt_pk_f32_fp8_sdwa v[12:13], v0 src0_sel:WORD_1
	v_cvt_pk_f32_fp8_e32 v[14:15], v1
	v_cvt_pk_f32_fp8_sdwa v[0:1], v1 src0_sel:WORD_1
	v_mov_b32_e32 v17, v4
	v_mov_b32_e32 v4, v11
	v_mov_b32_e32 v16, v10
	v_mov_b32_e32 v10, v12
	v_mov_b32_e32 v11, v6
	v_mov_b32_e32 v6, v13
	v_mov_b32_e32 v12, v14
	v_mov_b32_e32 v13, v8
	v_mov_b32_e32 v8, v15
	v_mov_b32_e32 v14, v0
	v_mov_b32_e32 v15, v2
	v_mov_b32_e32 v2, v1
	v_pk_mul_f32 v[0:1], v[4:5], v[4:5]
	s_nop 0
	v_pk_fma_f32 v[0:1], v[16:17], v[16:17], v[0:1]
	s_nop 0
	v_pk_fma_f32 v[0:1], v[10:11], v[10:11], v[0:1]
	s_nop 0
	v_pk_fma_f32 v[0:1], v[6:7], v[6:7], v[0:1]
	s_nop 0
	v_pk_fma_f32 v[0:1], v[12:13], v[12:13], v[0:1]
	s_nop 0
	v_pk_fma_f32 v[0:1], v[8:9], v[8:9], v[0:1]
	s_nop 0
	v_pk_fma_f32 v[0:1], v[14:15], v[14:15], v[0:1]
	s_nop 0
	v_pk_fma_f32 v[0:1], v[2:3], v[2:3], v[0:1]
	ds_bpermute_b32 v3, v118, v1
	ds_bpermute_b32 v2, v118, v0
	s_waitcnt lgkmcnt(0)
	v_pk_add_f32 v[0:1], v[0:1], v[2:3]
	ds_bpermute_b32 v3, v119, v1
	ds_bpermute_b32 v2, v119, v0
	s_waitcnt lgkmcnt(0)
	v_pk_add_f32 v[0:1], v[0:1], v[2:3]
	ds_bpermute_b32 v3, v120, v1
	ds_bpermute_b32 v2, v120, v0
	s_waitcnt lgkmcnt(0)
	v_pk_add_f32 v[0:1], v[0:1], v[2:3]
	ds_bpermute_b32 v3, v121, v1
	ds_bpermute_b32 v2, v121, v0
	s_waitcnt lgkmcnt(0)
	v_pk_add_f32 v[0:1], v[0:1], v[2:3]
	ds_bpermute_b32 v3, v122, v1
	ds_bpermute_b32 v2, v122, v0
	s_waitcnt lgkmcnt(0)
	v_pk_add_f32 v[0:1], v[0:1], v[2:3]
	ds_bpermute_b32 v3, v123, v1
	ds_bpermute_b32 v2, v123, v0
	s_and_saveexec_b64 s[12:13], s[4:5]
	s_cbranch_execz .LBB0_234
	s_waitcnt lgkmcnt(0)
	v_pk_add_f32 v[0:1], v[0:1], v[2:3]
	s_add_u32 s14, s28, s52
	v_pk_fma_f32 v[0:1], v[0:1], s[46:47], v[110:111] op_sel_hi:[1,0,0]
	s_addc_u32 s15, s29, s53
	v_mul_f32_e32 v2, 0x4b800000, v1
	v_cmp_gt_f32_e32 vcc, s1, v1
	v_cmp_gt_f32_e64 s[10:11], s1, v0
	s_nop 0
	v_cndmask_b32_e32 v1, v1, v2, vcc
	v_rsq_f32_e32 v1, v1
	v_mul_f32_e32 v2, 0x4b800000, v0
	v_cndmask_b32_e64 v0, v0, v2, s[10:11]
	v_rsq_f32_e32 v0, v0
	v_mul_f32_e32 v2, 0x45800000, v1
	v_cndmask_b32_e32 v1, v1, v2, vcc
	global_store_dword v125, v1, s[14:15]
	v_mul_f32_e32 v1, 0x45800000, v0
	v_cndmask_b32_e64 v0, v0, v1, s[10:11]
	global_store_dword v126, v0, s[14:15]
.LBB0_234:
	s_or_b64 exec, exec, s[12:13]
	v_mov_b32_e32 v0, v225
	v_cvt_f32_i32_e32 v0, v0
	v_mul_f32_e32 v0, v111, v0
	v_and_b32_e32 v1, 0x7fffffff, v0
	v_cmp_nlt_f32_e64 s[10:11], |v0|, s3
	s_and_saveexec_b64 s[12:13], s[10:11]
	s_xor_b64 s[54:55], exec, s[12:13]
	s_cbranch_execz .LBB0_236
	s_waitcnt lgkmcnt(0)
	v_lshrrev_b32_e32 v2, 23, v1
	v_add_u32_e32 v2, 0xffffff88, v2
	v_cmp_lt_u32_e32 vcc, 63, v2
	s_nop 1
	v_cndmask_b32_e32 v3, 0, v129, vcc
	v_add_u32_e32 v2, v3, v2
	v_cmp_lt_u32_e64 s[10:11], 31, v2
	s_nop 1
	v_cndmask_b32_e64 v3, 0, v130, s[10:11]
	v_add_u32_e32 v2, v3, v2
	v_cmp_lt_u32_e64 s[12:13], 31, v2
	s_nop 1
	v_cndmask_b32_e64 v3, 0, v130, s[12:13]
	v_add_u32_e32 v16, v3, v2
	v_and_b32_e32 v2, 0x7fffff, v1
	v_or_b32_e32 v14, 0x800000, v2
	v_mad_u64_u32 v[2:3], s[14:15], v14, s8, 0
	v_mov_b32_e32 v36, v3
	v_mad_u64_u32 v[4:5], s[14:15], v14, s9, v[36:37]
	v_mov_b32_e32 v36, v5
	v_mad_u64_u32 v[6:7], s[14:15], v14, s17, v[36:37]
	v_mov_b32_e32 v36, v7
	v_mad_u64_u32 v[8:9], s[14:15], v14, s19, v[36:37]
	v_mov_b32_e32 v36, v9
	v_mad_u64_u32 v[10:11], s[14:15], v14, s30, v[36:37]
	v_mov_b32_e32 v36, v11
	v_mad_u64_u32 v[12:13], s[14:15], v14, s31, v[36:37]
	v_mov_b32_e32 v36, v13
	v_mad_u64_u32 v[14:15], s[14:15], v14, s35, v[36:37]
	v_cndmask_b32_e32 v3, v12, v8, vcc
	v_cndmask_b32_e32 v5, v14, v10, vcc
	v_cndmask_b32_e32 v9, v15, v12, vcc
	v_cndmask_b32_e64 v7, v5, v3, s[10:11]
	v_cndmask_b32_e64 v5, v9, v5, s[10:11]
	v_cndmask_b32_e32 v9, v10, v6, vcc
	v_cndmask_b32_e64 v3, v3, v9, s[10:11]
	v_cndmask_b32_e32 v4, v8, v4, vcc
	v_cndmask_b32_e64 v5, v5, v7, s[12:13]
	v_cndmask_b32_e64 v7, v7, v3, s[12:13]
	v_sub_u32_e32 v10, 32, v16
	v_cndmask_b32_e64 v8, v9, v4, s[10:11]
	v_alignbit_b32 v11, v5, v7, v10
	v_cmp_eq_u32_e64 s[14:15], 0, v16
	v_cndmask_b32_e64 v3, v3, v8, s[12:13]
	v_alignbit_b32 v9, v7, v3, v10
	v_cndmask_b32_e64 v5, v11, v5, s[14:15]
	v_cndmask_b32_e32 v2, v6, v2, vcc
	v_cndmask_b32_e64 v7, v9, v7, s[14:15]
	v_bfe_u32 v12, v5, 29, 1
	v_cndmask_b32_e64 v2, v4, v2, s[10:11]
	v_alignbit_b32 v9, v5, v7, 30
	v_sub_u32_e32 v13, 0, v12
	v_cndmask_b32_e64 v2, v8, v2, s[12:13]
	v_xor_b32_e32 v9, v9, v13
	v_alignbit_b32 v4, v3, v2, v10
	v_cndmask_b32_e64 v3, v4, v3, s[14:15]
	v_ffbh_u32_e32 v6, v9
	v_alignbit_b32 v4, v7, v3, 30
	v_min_u32_e32 v6, 32, v6
	v_alignbit_b32 v2, v3, v2, 30
	v_xor_b32_e32 v4, v4, v13
	v_sub_u32_e32 v7, 31, v6
	v_xor_b32_e32 v2, v2, v13
	v_alignbit_b32 v8, v9, v4, v7
	v_alignbit_b32 v2, v4, v2, v7
	v_alignbit_b32 v3, v8, v2, 9
	v_ffbh_u32_e32 v4, v3
	v_min_u32_e32 v4, 32, v4
	v_lshrrev_b32_e32 v11, 29, v5
	v_not_b32_e32 v7, v4
	v_alignbit_b32 v2, v3, v2, v7
	v_lshlrev_b32_e32 v3, 31, v11
	v_or_b32_e32 v7, 0x33000000, v3
	v_add_lshl_u32 v4, v4, v6, 23
	v_lshrrev_b32_e32 v2, 9, v2
	v_sub_u32_e32 v4, v7, v4
	v_or_b32_e32 v3, 0.5, v3
	v_lshlrev_b32_e32 v6, 23, v6
	v_or_b32_e32 v2, v4, v2
	v_lshrrev_b32_e32 v4, 9, v8
	v_sub_u32_e32 v3, v3, v6
	v_or_b32_e32 v3, v4, v3
	v_mul_f32_e32 v4, 0x3fc90fda, v3
	v_fma_f32 v6, v3, s37, -v4
	v_fmac_f32_e32 v6, 0x33a22168, v3
	v_fmac_f32_e32 v6, 0x3fc90fda, v2
	v_lshrrev_b32_e32 v3, 30, v5
	v_add_f32_e32 v2, v4, v6
	v_add_u32_e32 v3, v12, v3

; __device__ __forceinline__ unsigned cvt_pk4_fp8(float a, float b, float c, float d) { int w; asm("" : "=v"(w));     w = __builtin_amdgcn_cvt_pk_fp8_f32(a, b, w, false); w = __builtin_amdgcn_cvt_pk_fp8_f32(c, d, w, true); return (unsigned)w; }
; __global__ void __launch_bounds__(512, 2) fwd_kernel(Params p) {
;     ...
;                     float z1 = 0.f, z2 = 0.f;
; #pragma unroll
;                     for (int q = 0; q < 4; ++q) { z1 += zk[(q * 64 + tl) * 65 + i]; z2 += zk[(q * 64 + tl) * 65 + 32 + i]; }
;                     float sm = (lane < 32) ? (z1 * z1 + z2 * z2) : 0.f;
;                     const float rstd = rsqrtf(wave_sum(sm) * (1.f / 64.f) + RMS_EPS);
;                     const float t1 = z1 * (rstd * att::KSC) * p.in[I_GKR][i], t2 = z2 * (rstd * att::KSC) * p.in[I_GKR][32 + i];
;                     const float o1 = t1 * cs - t2 * sn, o2 = t2 * cs + t1 * sn;
;                     const unsigned pk = cvt_pk4_fp8(o1, o2, 0.f, 0.f);
;                     const int pp1 = 32 * ((i >> 3) & 1) + 8 * (i >> 4) + (i & 7);
;                     if (lane < 32) { KPE8[(size_t)m * 64 + pp1] = (unsigned char)(pk & 0xffu); KPE8[(size_t)m * 64 + pp1 + 16] = (unsigned char)((pk >> 8) & 0xffu); }
.LBB0_240:
	s_or_b64 exec, exec, s[10:11]
	v_add_u32_e32 v6, s27, v43
	ds_read2_b32 v[2:3], v6 offset1:32
	v_add_u32_e32 v4, 0x4000, v6
	v_add_u32_e32 v7, 0x8000, v6
	ds_read2_b32 v[4:5], v4 offset0:64 offset1:96
	v_add_u32_e32 v6, 0xc000, v6
	s_waitcnt lgkmcnt(1)
	v_add_f32_e32 v8, 0, v2
	v_add_f32_e32 v9, 0, v3
	ds_read2_b32 v[2:3], v7 offset0:128 offset1:160
	ds_read2_b32 v[6:7], v6 offset0:192 offset1:224
	s_waitcnt lgkmcnt(2)
	v_add_f32_e32 v4, v8, v4
	v_add_f32_e32 v5, v9, v5
	s_waitcnt lgkmcnt(1)
	v_add_f32_e32 v2, v4, v2
	v_add_f32_e32 v4, v5, v3
	s_waitcnt lgkmcnt(0)
	v_add_f32_e32 v3, v2, v6
	v_add_f32_e32 v4, v4, v7
	v_mul_f32_e32 v2, v3, v3
	v_fmac_f32_e32 v2, v4, v4
	v_cndmask_b32_e64 v2, 0, v2, s[6:7]
	ds_bpermute_b32 v5, v118, v2
	s_waitcnt lgkmcnt(0)
	v_add_f32_e32 v2, v2, v5
	ds_bpermute_b32 v5, v119, v2
	s_waitcnt lgkmcnt(0)
	v_add_f32_e32 v2, v2, v5
	ds_bpermute_b32 v5, v120, v2
	s_waitcnt lgkmcnt(0)
	v_add_f32_e32 v2, v2, v5
	ds_bpermute_b32 v5, v121, v2
	s_waitcnt lgkmcnt(0)
	v_add_f32_e32 v2, v2, v5
	ds_bpermute_b32 v5, v122, v2
	s_waitcnt lgkmcnt(0)
	v_add_f32_e32 v5, v2, v5
	ds_bpermute_b32 v6, v123, v5
	s_and_saveexec_b64 s[10:11], s[6:7]
	s_cbranch_execz .LBB0_231
	v_mov_b32_e32 v7, v228
	v_mov_b32_e32 v8, v229
	s_waitcnt lgkmcnt(0)
	v_add_f32_e32 v5, v5, v6
	v_fmamk_f32 v5, v5, 0x3c800000, v110
	v_mul_f32_e32 v6, 0x4b800000, v5
	v_cmp_gt_f32_e32 vcc, s1, v5
	s_nop 1
	v_cndmask_b32_e32 v5, v5, v6, vcc
	v_rsq_f32_e32 v5, v5
	s_nop 0
	v_mul_f32_e32 v6, 0x45800000, v5
	v_cndmask_b32_e32 v5, v5, v6, vcc
	v_mul_f32_e32 v5, 0x3ed53b94, v5
	v_mul_f32_e32 v4, v4, v5
	v_mul_f32_e32 v3, v3, v5
	v_mul_f32_e32 v3, v3, v7
	v_mul_f32_e32 v4, v4, v8
	v_mul_f32_e32 v5, v0, v4
	v_mul_f32_e32 v4, v1, v4
	v_fma_f32 v1, v1, v3, -v5
	v_fmac_f32_e32 v4, v0, v3
	v_cvt_pk_fp8_f32 v2, v1, v4
	v_lshl_add_u64 v[0:1], s[28:29], 0, v[114:115]
	v_add_co_u32_e32 v0, vcc, 0x3600000, v0
	v_cvt_pk_fp8_f32 v2, 0, 0 op_sel:[0,0,1]
	s_nop 0
	v_addc_co_u32_e32 v1, vcc, 0, v1, vcc
	global_store_byte v[0:1], v2, off
	v_lshrrev_b32_e32 v2, 8, v2
	global_store_byte v[0:1], v2, off offset:16
	s_branch .LBB0_231
